# baseline (speedup 1.0000x reference)
_Z13router_kernelPKfS0_S0_PcPfS1_:
	s_load_dwordx2 s[98:99], s[0:1], 0x0
	s_load_dwordx2 s[24:25], s[0:1], 0x10
	v_writelane_b32 v238, s0, 0
	s_load_dwordx2 s[4:5], s[0:1], 0x28
	v_lshrrev_b32_e32 v37, 6, v0
	v_writelane_b32 v238, s1, 1
	v_bfe_u32 v2, v0, 4, 2
	v_bitop3_b32 v39, v2, v0, 15 bitop3:0x78
	s_waitcnt lgkmcnt(0)
	v_writelane_b32 v238, s4, 2
	v_and_b32_e32 v36, 15, v0
	v_bitop3_b32 v41, v2, v36, 4 bitop3:0x36
	v_writelane_b32 v238, s5, 3
	s_lshl_b32 s4, s2, 7
	v_lshl_or_b32 v1, v37, 4, s4
	v_or_b32_e32 v38, v2, v1
	s_movk_i32 s4, 0xc40
	v_mul_lo_u32 v3, v38, s4
	v_lshl_add_u32 v214, v39, 4, v3
	v_or_b32_e32 v3, 4, v2
	v_or_b32_e32 v40, v3, v1
	v_mul_lo_u32 v3, v40, s4
	v_lshl_add_u32 v215, v41, 4, v3
	v_or_b32_e32 v3, 8, v2
	v_or_b32_e32 v42, v3, v1
	v_mul_lo_u32 v3, v42, s4
	v_bitop3_b32 v43, v2, v36, 8 bitop3:0x36
	v_lshl_add_u32 v216, v43, 4, v3
	v_or_b32_e32 v3, 12, v2
	v_or_b32_e32 v44, v3, v1
	v_and_b32_e32 v200, 63, v0
	v_mul_lo_u32 v3, v44, s4
	v_bitop3_b32 v45, v2, v36, 12 bitop3:0x36
	v_readfirstlane_b32 s4, v37
	v_lshl_add_u32 v217, v45, 4, v3
	s_cmp_ge_u32 s4, 4
	s_cbranch_scc0 .Lrt_noprio
	s_setprio 1
.Lrt_noprio:
	s_cmpk_gt_i32 s4, 0x61
	v_lshlrev_b32_e32 v198, 4, v200
	v_writelane_b32 v238, s2, 4
	global_load_dwordx4 v[30:33], v214, s[98:99] offset:0 nt
	global_load_dwordx4 v[26:29], v215, s[98:99] offset:0 nt
	global_load_dwordx4 v[22:25], v216, s[98:99] offset:0 nt
	global_load_dwordx4 v[18:21], v217, s[98:99] offset:0 nt
	global_load_dwordx4 v[14:17], v214, s[98:99] offset:0x100 nt
	global_load_dwordx4 v[10:13], v215, s[98:99] offset:0x100 nt
	global_load_dwordx4 v[6:9], v216, s[98:99] offset:0x100 nt
	global_load_dwordx4 v[2:5], v217, s[98:99] offset:0x100 nt
	global_load_dwordx4 v[62:65], v214, s[98:99] offset:0x200 nt
	global_load_dwordx4 v[58:61], v215, s[98:99] offset:0x200 nt
	global_load_dwordx4 v[54:57], v216, s[98:99] offset:0x200 nt
	global_load_dwordx4 v[50:53], v217, s[98:99] offset:0x200 nt
	global_load_dwordx4 v[78:81], v214, s[98:99] offset:0x300 nt
	global_load_dwordx4 v[74:77], v215, s[98:99] offset:0x300 nt
	global_load_dwordx4 v[70:73], v216, s[98:99] offset:0x300 nt
	global_load_dwordx4 v[66:69], v217, s[98:99] offset:0x300 nt
	global_load_dwordx4 v[94:97], v214, s[98:99] offset:0x400 nt
	global_load_dwordx4 v[90:93], v215, s[98:99] offset:0x400 nt
	global_load_dwordx4 v[86:89], v216, s[98:99] offset:0x400 nt
	global_load_dwordx4 v[82:85], v217, s[98:99] offset:0x400 nt
	global_load_dwordx4 v[110:113], v214, s[98:99] offset:0x500 nt
	global_load_dwordx4 v[106:109], v215, s[98:99] offset:0x500 nt
	global_load_dwordx4 v[102:105], v216, s[98:99] offset:0x500 nt
	global_load_dwordx4 v[98:101], v217, s[98:99] offset:0x500 nt
	s_cbranch_scc1 .LBB1_3
	v_readlane_b32 s0, v238, 0
	v_readlane_b32 s1, v238, 1
	s_load_dwordx2 s[8:9], s[0:1], 0x18
	v_mov_b32_e32 v199, 0
	s_mov_b64 s[10:11], 0x4000
	s_add_i32 s6, s4, -8
	s_lshl_b32 s4, s4, 10
	s_waitcnt lgkmcnt(0)
	v_lshl_add_u64 v[34:35], s[8:9], 0, v[198:199]
	v_lshl_add_u64 v[34:35], v[34:35], 0, s[10:11]
